# attention K rows gathered coalesced (8 keys x 128 B per load, V-pattern addresses) and transposed to the MFMA operand layout through a per-wave 4 KB swizzled LDS area; on top of v11
# speedup vs baseline: 1.0834x; 1.0596x over previous
.LBB0_718:
	s_or_b64 exec, exec, s[12:13]
	s_cmp_eq_u32 s18, 2
	s_cselect_b32 s18, 32, 16
	s_lshl_b32 s12, s44, 9
	s_add_i32 s12, s12, 0
	v_lshlrev_b64 v[56:57], 1, v[14:15]
	v_lshl_add_u64 v[2:3], s[42:43], 0, v[56:57]
	s_waitcnt vmcnt(0)
	v_and_b32_e32 v199, 0x70, v52
	v_mov_b32_e32 v0, v199
	v_lshl_add_u64 v[212:213], s[42:43], 0, v[0:1]
	v_lshl_add_u32 v70, v233, 1, s12
	ds_read_u16 v46, v70 offset:32768
	ds_read_u16 v50, v70 offset:32784
	ds_read_u16 v62, v70 offset:32800
	ds_read_u16 v66, v70 offset:32816
	ds_read_u16 v71, v70 offset:32832
	ds_read_u16 v74, v70 offset:32848
	ds_read_u16 v78, v70 offset:32864
	ds_read_u16 v82, v70 offset:32880
	s_waitcnt lgkmcnt(7)
	v_lshlrev_b32_e32 v0, 9, v46
	v_lshl_add_u64 v[46:47], v[212:213], 0, v[0:1]
	global_load_dwordx4 v[14:17], v[46:47], off
	s_waitcnt lgkmcnt(6)
	v_lshlrev_b32_e32 v0, 9, v50
	v_lshl_add_u64 v[50:51], v[212:213], 0, v[0:1]
	global_load_dwordx4 v[18:21], v[50:51], off
	s_waitcnt lgkmcnt(5)
	v_lshlrev_b32_e32 v0, 9, v62
	v_lshl_add_u64 v[62:63], v[212:213], 0, v[0:1]
	global_load_dwordx4 v[22:25], v[62:63], off
	s_waitcnt lgkmcnt(4)
	v_lshlrev_b32_e32 v0, 9, v66
	v_lshl_add_u64 v[66:67], v[212:213], 0, v[0:1]
	global_load_dwordx4 v[26:29], v[66:67], off
	s_waitcnt lgkmcnt(3)
	v_lshlrev_b32_e32 v0, 9, v71
	v_lshl_add_u64 v[70:71], v[212:213], 0, v[0:1]
	global_load_dwordx4 v[30:33], v[70:71], off
	s_waitcnt lgkmcnt(2)
	v_lshlrev_b32_e32 v0, 9, v74
	v_lshl_add_u64 v[74:75], v[212:213], 0, v[0:1]
	global_load_dwordx4 v[34:37], v[74:75], off
	s_waitcnt lgkmcnt(1)
	v_lshlrev_b32_e32 v0, 9, v78
	v_lshl_add_u64 v[78:79], v[212:213], 0, v[0:1]
	global_load_dwordx4 v[38:41], v[78:79], off
	s_waitcnt lgkmcnt(0)
	v_lshlrev_b32_e32 v0, 9, v82
	v_lshl_add_u64 v[82:83], v[212:213], 0, v[0:1]
	global_load_dwordx4 v[42:45], v[82:83], off
	global_load_dwordx4 v[46:49], v[46:47], off offset:128
	s_nop 0
	global_load_dwordx4 v[50:53], v[50:51], off offset:128
	s_nop 0
	global_load_dwordx4 v[62:65], v[62:63], off offset:128
	s_nop 0
	global_load_dwordx4 v[66:69], v[66:67], off offset:128
	s_nop 0
	global_load_dwordx4 v[70:73], v[70:71], off offset:128
	s_nop 0
	global_load_dwordx4 v[74:77], v[74:75], off offset:128
	s_nop 0
	global_load_dwordx4 v[78:81], v[78:79], off offset:128
	s_nop 0
	global_load_dwordx4 v[82:85], v[82:83], off offset:128
	v_mov_b32_e32 v0, v199
	v_lshlrev_b32_e32 v5, 6, v5
	s_mov_b32 s47, 2
	v_lshlrev_b32_e32 v210, 2, v54
	v_lshlrev_b32_e32 v54, 4, v233
	v_and_b32_e32 v54, 0x60, v54
	v_xad_u32 v61, v54, v0, s82
	v_lshrrev_b32_e32 v54, 2, v232
	v_or_b32_e32 v54, v210, v54
	v_and_b32_e32 v55, 24, v55
	v_lshlrev_b32_e32 v58, 4, v54
	v_lshl_add_u32 v87, v54, 7, s82
	v_add_u32_e32 v54, 16, v54
	v_lshlrev_b32_e32 v59, 4, v54
	v_lshl_add_u32 v89, v54, 7, s82
	v_or_b32_e32 v92, 32, v55
	s_movk_i32 s12, 0x60
	v_or_b32_e32 v94, 64, v55
	v_lshl_add_u64 v[212:213], s[42:43], 0, v[0:1]
	v_lshlrev_b32_e32 v0, 1, v5
	v_lshlrev_b32_e32 v60, 7, v233
	v_and_b32_e32 v86, 0x60, v58
	v_and_b32_e32 v88, 0x60, v59
	v_lshlrev_b32_e32 v54, 6, v232
	v_add_u32_e32 v90, v87, v55
	v_add_u32_e32 v91, v89, v55
	v_bitop3_b32 v93, v58, v92, s12 bitop3:0x6c
	v_bitop3_b32 v92, v59, v92, s12 bitop3:0x6c
	v_bitop3_b32 v95, v58, v94, s12 bitop3:0x6c
	v_bitop3_b32 v94, v59, v94, s12 bitop3:0x6c
	v_bitop3_b32 v96, v58, v55, s12 bitop3:0x4e
	v_bitop3_b32 v55, v59, v55, s12 bitop3:0x4e
	v_lshl_add_u64 v[58:59], s[74:75], 0, v[0:1]
	v_mov_b32_e32 v244, 0
	v_ashrrev_i32_e32 v211, 31, v210
	v_lshl_add_u64 v[214:215], v[58:59], 0, v[56:57]
	v_mov_b32_e32 v202, 0xf149f2ca
	v_lshlrev_b32_e32 v216, 1, v54
	v_mov_b32_e32 v5, v4
	v_add_u32_e32 v235, v61, v60
	v_add_u32_e32 v236, v90, v86
	v_add_u32_e32 v237, v91, v88
	v_add_u32_e32 v238, v87, v93
	v_add_u32_e32 v239, v89, v92
	v_add_u32_e32 v240, v87, v95
	v_add_u32_e32 v241, v89, v94
	v_add_u32_e32 v242, v87, v96
	v_add_u32_e32 v243, v89, v55
	v_mov_b32_e32 v154, 0
	v_mov_b32_e32 v155, v244
	v_mov_b32_e32 v156, v244
	v_mov_b32_e32 v157, v244
	v_mov_b32_e32 v158, 0
	v_mov_b32_e32 v159, v244
	v_mov_b32_e32 v160, v244
	v_mov_b32_e32 v161, v244
	v_mov_b32_e32 v162, 0
	v_mov_b32_e32 v163, v244
	v_mov_b32_e32 v164, v244
	v_mov_b32_e32 v165, v244
	v_mov_b32_e32 v166, 0
	v_mov_b32_e32 v167, v244
	v_mov_b32_e32 v168, v244
	v_mov_b32_e32 v169, v244
	v_lshrrev_b32_e32 v196, 1, v233
	v_and_b32_e32 v197, 7, v232
	v_xor_b32_e32 v196, v196, v197
	v_lshlrev_b32_e32 v196, 4, v196
	v_lshl_add_u32 v196, v233, 7, v196
	s_lshl_b32 s12, s96, 12
	s_add_i32 s12, s12, 0x10000
	v_add_u32_e32 v196, s12, v196
	v_xor_b32_e32 v197, 64, v196
	v_lshrrev_b32_e32 v198, 1, v232
	v_lshrrev_b32_e32 v199, 1, v233
	v_xor_b32_e32 v198, v198, v199
	v_lshlrev_b32_e32 v198, 4, v198
	v_lshl_add_u32 v198, v232, 7, v198
	v_add_u32_e32 v198, s12, v198
	v_xor_b32_e32 v199, 64, v198
	s_branch .LBB0_720

.LBB0_720:
	s_add_i32 s12, s47, -2
	s_lshr_b32 s42, s12, 2
	s_add_i32 s42, s42, s44
	s_and_b32 s34, s12, 2
	s_lshl_b32 s12, s42, 9
	s_add_i32 s43, s12, 0
	s_lshl_b32 s12, s34, 7
	s_add_i32 s43, s43, s12
	v_lshl_add_u32 v90, v233, 1, s43
	ds_read_u16 v102, v90 offset:32896
	ds_read_u16 v106, v90 offset:32912
	ds_read_u16 v110, v90 offset:32928
	ds_read_u16 v114, v90 offset:32944
	ds_read_u16 v86, v90 offset:32960
	ds_read_u16 v91, v90 offset:32976
	ds_read_u16 v94, v90 offset:32992
	ds_read_u16 v98, v90 offset:33008
	s_waitcnt lgkmcnt(7)
	v_lshlrev_b32_e32 v0, 9, v102
	v_lshl_add_u64 v[102:103], v[212:213], 0, v[0:1]
	global_load_dwordx4 v[138:141], v[102:103], off
	s_waitcnt lgkmcnt(6)
	v_lshlrev_b32_e32 v0, 9, v106
	v_lshl_add_u64 v[106:107], v[212:213], 0, v[0:1]
	global_load_dwordx4 v[142:145], v[106:107], off
	s_waitcnt lgkmcnt(5)
	v_lshlrev_b32_e32 v0, 9, v110
	v_lshl_add_u64 v[110:111], v[212:213], 0, v[0:1]
	global_load_dwordx4 v[146:149], v[110:111], off
	s_waitcnt lgkmcnt(4)
	v_lshlrev_b32_e32 v0, 9, v114
	v_lshl_add_u64 v[114:115], v[212:213], 0, v[0:1]
	global_load_dwordx4 v[134:137], v[114:115], off
	s_waitcnt lgkmcnt(3)
	v_lshlrev_b32_e32 v0, 9, v86
	v_lshl_add_u64 v[86:87], v[212:213], 0, v[0:1]
	global_load_dwordx4 v[130:133], v[86:87], off
	s_waitcnt lgkmcnt(2)
	v_lshlrev_b32_e32 v0, 9, v91
	v_lshl_add_u64 v[90:91], v[212:213], 0, v[0:1]
	global_load_dwordx4 v[126:129], v[90:91], off
	s_waitcnt lgkmcnt(1)
	v_lshlrev_b32_e32 v0, 9, v94
	v_lshl_add_u64 v[94:95], v[212:213], 0, v[0:1]
	global_load_dwordx4 v[122:125], v[94:95], off
	s_waitcnt lgkmcnt(0)
	v_lshlrev_b32_e32 v0, 9, v98
	v_lshl_add_u64 v[98:99], v[212:213], 0, v[0:1]
	global_load_dwordx4 v[118:121], v[98:99], off
	global_load_dwordx4 v[102:105], v[102:103], off offset:128
	s_nop 0
	global_load_dwordx4 v[106:109], v[106:107], off offset:128
	s_nop 0
	global_load_dwordx4 v[110:113], v[110:111], off offset:128
	s_nop 0
	global_load_dwordx4 v[114:117], v[114:115], off offset:128
	s_nop 0
	global_load_dwordx4 v[86:89], v[86:87], off offset:128
	s_nop 0
	global_load_dwordx4 v[90:93], v[90:91], off offset:128
	s_nop 0
	global_load_dwordx4 v[94:97], v[94:95], off offset:128
	s_nop 0
	global_load_dwordx4 v[98:101], v[98:99], off offset:128
	s_cmp_eq_u32 s34, 0
	s_cselect_b64 s[30:31], -1, 0
	s_cmp_lg_u32 s34, 0
	s_cbranch_scc1 .LBB0_722
	v_mov_b32_e32 v244, 0
	v_mov_b32_e32 v202, 0xf149f2ca
	v_mov_b32_e32 v154, 0
	v_mov_b32_e32 v155, v244
	v_mov_b32_e32 v156, v244
	v_mov_b32_e32 v157, v244
	v_mov_b32_e32 v158, 0
	v_mov_b32_e32 v159, v244
	v_mov_b32_e32 v160, v244
	v_mov_b32_e32 v161, v244
	v_mov_b32_e32 v162, 0
	v_mov_b32_e32 v163, v244
	v_mov_b32_e32 v164, v244
	v_mov_b32_e32 v165, v244
	v_mov_b32_e32 v166, 0
	v_mov_b32_e32 v167, v244
	v_mov_b32_e32 v168, v244
	v_mov_b32_e32 v169, v244

.LBB0_736:
	s_waitcnt vmcnt(24)
	ds_write_b128 v196, v[14:17]
	ds_write_b128 v197, v[18:21] offset:1024
	ds_write_b128 v196, v[22:25] offset:2048
	ds_write_b128 v197, v[26:29] offset:3072
	ds_read_b128 v[14:17], v198
	ds_read_b128 v[18:21], v199
	ds_read_b128 v[22:25], v198 offset:2048
	ds_read_b128 v[26:29], v199 offset:2048
	ds_write_b128 v196, v[30:33]
	ds_write_b128 v197, v[34:37] offset:1024
	ds_write_b128 v196, v[38:41] offset:2048
	ds_write_b128 v197, v[42:45] offset:3072
	ds_read_b128 v[30:33], v198
	ds_read_b128 v[34:37], v199
	ds_read_b128 v[38:41], v198 offset:2048
	ds_read_b128 v[42:45], v199 offset:2048
	s_waitcnt lgkmcnt(0)
	s_waitcnt vmcnt(31)
	v_mfma_f32_16x16x32_bf16 v[170:173], v[14:17], v[6:9], v[170:173]
	s_mov_b32 s12, 0x40c00000
	s_waitcnt vmcnt(30)
	v_mfma_f32_16x16x32_bf16 v[182:185], v[18:21], v[10:13], v[170:173]
	s_waitcnt vmcnt(29)
	v_mfma_f32_16x16x32_bf16 v[170:173], v[22:25], v[6:9], v[174:177]
	s_waitcnt vmcnt(28)
	v_mfma_f32_16x16x32_bf16 v[178:181], v[26:29], v[10:13], v[170:173]
	s_nop 3
	v_max_f32_e32 v0, v185, v185
	v_max_f32_e32 v153, v184, v184
	v_max_f32_e32 v0, v153, v0
	s_waitcnt vmcnt(27)
	v_mfma_f32_16x16x32_bf16 v[170:173], v[30:33], v[6:9], v[186:189]
	v_max3_f32 v0, v182, v183, v0
	v_max_f32_e32 v153, v181, v181
	s_waitcnt vmcnt(26)
	v_mfma_f32_16x16x32_bf16 v[174:177], v[34:37], v[10:13], v[170:173]
	v_max_f32_e32 v186, v180, v180
	v_max_f32_e32 v153, v186, v153
	v_max3_f32 v153, v178, v179, v153
	s_waitcnt vmcnt(25) lgkmcnt(0)
	v_mfma_f32_16x16x32_bf16 v[170:173], v[38:41], v[6:9], v[190:193]
	s_waitcnt vmcnt(24)
	v_mfma_f32_16x16x32_bf16 v[170:173], v[42:45], v[10:13], v[170:173]
	s_nop 0
	v_max_f32_e32 v186, v175, v175
	v_max_f32_e32 v187, v174, v174
	v_max_f32_e32 v186, v187, v186
	v_max_f32_e32 v187, v177, v177
	v_max_f32_e32 v188, v176, v176
	v_max_f32_e32 v187, v188, v187
	s_nop 0
	v_max_f32_e32 v188, v173, v173
	v_max_f32_e32 v189, v172, v172
	v_max_f32_e32 v188, v189, v188
	v_max3_f32 v188, v170, v171, v188
	v_max3_f32 v186, v186, v187, v188
	v_max3_f32 v0, v0, v153, v186
	v_mov_b32_e32 v153, v0
	s_nop 1
	v_permlane16_swap_b32_e32 v0, v153
	v_max_f32_e32 v153, v153, v153
	v_max_f32_e32 v0, v0, v0
	v_max_f32_e32 v0, v0, v153
	v_mov_b32_e32 v153, v0
	s_nop 1
	v_permlane32_swap_b32_e32 v0, v153
	v_max_f32_e32 v153, v153, v153
	v_max_f32_e32 v0, v0, v0
	v_max_f32_e32 v0, v0, v153
	v_sub_f32_e32 v153, v0, v202
	v_mul_f32_e32 v153, 0x3e38aa3b, v153
	v_cmp_lt_f32_e32 vcc, s12, v153
	s_cbranch_vccz .LBB0_738
	v_max_f32_e32 v0, v0, v0
	v_max_f32_e32 v153, v202, v202
	v_max_f32_e32 v153, v153, v0
	v_sub_f32_e32 v0, v202, v153
	v_mul_f32_e32 v0, 0x3e38aa3b, v0
	v_exp_f32_e32 v0, v0
	v_mov_b32_e32 v202, v153
	v_pk_mul_f32 v[168:169], v[168:169], v[0:1] op_sel_hi:[1,0]
	v_pk_mul_f32 v[166:167], v[166:167], v[0:1] op_sel_hi:[1,0]
	v_pk_mul_f32 v[164:165], v[164:165], v[0:1] op_sel_hi:[1,0]
	v_pk_mul_f32 v[162:163], v[162:163], v[0:1] op_sel_hi:[1,0]
	v_pk_mul_f32 v[160:161], v[160:161], v[0:1] op_sel_hi:[1,0]
	v_pk_mul_f32 v[158:159], v[158:159], v[0:1] op_sel_hi:[1,0]
	v_pk_mul_f32 v[156:157], v[156:157], v[0:1] op_sel_hi:[1,0]
	v_pk_mul_f32 v[154:155], v[154:155], v[0:1] op_sel_hi:[1,0]
	v_mul_f32_e32 v244, v244, v0

.LBB0_745:
	s_lshl_b32 s12, s35, 9
	s_add_i32 s12, s12, 0
	s_lshl_b32 s13, s34, 7
	s_add_i32 s12, s12, s13
	v_lshl_add_u32 v70, v233, 1, s12
	ds_read_u16 v46, v70 offset:32768
	ds_read_u16 v50, v70 offset:32784
	ds_read_u16 v62, v70 offset:32800
	ds_read_u16 v66, v70 offset:32816
	ds_read_u16 v71, v70 offset:32832
	ds_read_u16 v74, v70 offset:32848
	ds_read_u16 v78, v70 offset:32864
	ds_read_u16 v82, v70 offset:32880
	s_waitcnt lgkmcnt(7)
	v_lshlrev_b32_e32 v0, 9, v46
	v_lshl_add_u64 v[46:47], v[212:213], 0, v[0:1]
	global_load_dwordx4 v[14:17], v[46:47], off
	s_waitcnt lgkmcnt(6)
	v_lshlrev_b32_e32 v0, 9, v50
	v_lshl_add_u64 v[50:51], v[212:213], 0, v[0:1]
	global_load_dwordx4 v[18:21], v[50:51], off
	s_waitcnt lgkmcnt(5)
	v_lshlrev_b32_e32 v0, 9, v62
	v_lshl_add_u64 v[62:63], v[212:213], 0, v[0:1]
	global_load_dwordx4 v[22:25], v[62:63], off
	s_waitcnt lgkmcnt(4)
	v_lshlrev_b32_e32 v0, 9, v66
	v_lshl_add_u64 v[66:67], v[212:213], 0, v[0:1]
	global_load_dwordx4 v[26:29], v[66:67], off
	s_waitcnt lgkmcnt(3)
	v_lshlrev_b32_e32 v0, 9, v71
	v_lshl_add_u64 v[70:71], v[212:213], 0, v[0:1]
	global_load_dwordx4 v[30:33], v[70:71], off
	s_waitcnt lgkmcnt(2)
	v_lshlrev_b32_e32 v0, 9, v74
	v_lshl_add_u64 v[74:75], v[212:213], 0, v[0:1]
	global_load_dwordx4 v[34:37], v[74:75], off
	s_waitcnt lgkmcnt(1)
	v_lshlrev_b32_e32 v0, 9, v78
	v_lshl_add_u64 v[78:79], v[212:213], 0, v[0:1]
	global_load_dwordx4 v[38:41], v[78:79], off
	s_waitcnt lgkmcnt(0)
	v_lshlrev_b32_e32 v0, 9, v82
	v_lshl_add_u64 v[82:83], v[212:213], 0, v[0:1]
	global_load_dwordx4 v[42:45], v[82:83], off
	global_load_dwordx4 v[46:49], v[46:47], off offset:128
	s_nop 0
	global_load_dwordx4 v[50:53], v[50:51], off offset:128
	s_nop 0
	global_load_dwordx4 v[62:65], v[62:63], off offset:128
	s_nop 0
	global_load_dwordx4 v[66:69], v[66:67], off offset:128
	s_nop 0
	global_load_dwordx4 v[70:73], v[70:71], off offset:128
	s_nop 0
	global_load_dwordx4 v[74:77], v[74:75], off offset:128
	s_nop 0
	global_load_dwordx4 v[78:81], v[78:79], off offset:128
	s_nop 0
	global_load_dwordx4 v[82:85], v[82:83], off offset:128

.LBB0_760:
	s_waitcnt vmcnt(8)
	ds_write_b128 v196, v[138:141]
	ds_write_b128 v197, v[142:145] offset:1024
	ds_write_b128 v196, v[146:149] offset:2048
	ds_write_b128 v197, v[134:137] offset:3072
	ds_read_b128 v[138:141], v198
	ds_read_b128 v[142:145], v199
	ds_read_b128 v[146:149], v198 offset:2048
	ds_read_b128 v[134:137], v199 offset:2048
	ds_write_b128 v196, v[130:133]
	ds_write_b128 v197, v[126:129] offset:1024
	ds_write_b128 v196, v[122:125] offset:2048
	ds_write_b128 v197, v[118:121] offset:3072
	ds_read_b128 v[130:133], v198
	ds_read_b128 v[126:129], v199
	ds_read_b128 v[122:125], v198 offset:2048
	ds_read_b128 v[118:121], v199 offset:2048
	s_waitcnt lgkmcnt(0)
	s_waitcnt vmcnt(15)
	v_mfma_f32_16x16x32_bf16 v[138:141], v[138:141], v[6:9], v[150:153]
	v_add_f32_e32 v0, v182, v183
	s_mov_b32 s12, 0x40c00000
	s_waitcnt vmcnt(11)
	v_mfma_f32_16x16x32_bf16 v[130:133], v[130:133], v[6:9], v[174:177]
	s_waitcnt vmcnt(9) lgkmcnt(0)
	v_mfma_f32_16x16x32_bf16 v[122:125], v[122:125], v[6:9], v[178:181]
	v_mfma_f32_16x16x32_bf16 v[138:141], v[142:145], v[10:13], v[138:141]
	v_add_f32_e32 v142, v244, v0
	v_mfma_f32_16x16x32_bf16 v[144:147], v[146:149], v[6:9], v[170:173]
	v_mfma_f32_16x16x32_bf16 v[126:129], v[126:129], v[10:13], v[130:133]
	s_nop 4
	v_max_f32_e32 v0, v141, v141
	v_max_f32_e32 v143, v140, v140
	v_max_f32_e32 v0, v143, v0
	s_waitcnt vmcnt(8)
	v_mfma_f32_16x16x32_bf16 v[118:121], v[118:121], v[10:13], v[122:125]
	v_max3_f32 v0, v138, v139, v0
	v_max_f32_e32 v130, v127, v127
	v_max_f32_e32 v131, v126, v126
	v_mfma_f32_16x16x32_bf16 v[134:137], v[134:137], v[10:13], v[144:147]
	v_max_f32_e32 v130, v131, v130
	s_nop 2
	v_max_f32_e32 v122, v121, v121
	v_max_f32_e32 v123, v120, v120
	v_max_f32_e32 v131, v129, v129
	v_max_f32_e32 v132, v128, v128
	v_max_f32_e32 v143, v137, v137
	v_max_f32_e32 v144, v136, v136
	v_max_f32_e32 v122, v123, v122
	v_max_f32_e32 v143, v144, v143
	v_max_f32_e32 v131, v132, v131
	v_max3_f32 v122, v118, v119, v122
	v_max3_f32 v143, v134, v135, v143
	v_max3_f32 v122, v130, v131, v122
	v_max3_f32 v0, v0, v143, v122
	v_mov_b32_e32 v122, v0
	s_nop 1
	v_permlane16_swap_b32_e32 v0, v122
	v_max_f32_e32 v122, v122, v122
	v_max_f32_e32 v0, v0, v0
	v_max_f32_e32 v0, v0, v122
	v_mov_b32_e32 v122, v0
	s_nop 1
	v_permlane32_swap_b32_e32 v0, v122
	v_max_f32_e32 v122, v122, v122
	v_max_f32_e32 v0, v0, v0
	v_max_f32_e32 v0, v0, v122
	v_sub_f32_e32 v122, v0, v202
	v_mul_f32_e32 v122, 0x3e38aa3b, v122
	v_cmp_lt_f32_e32 vcc, s12, v122
	s_cbranch_vccz .LBB0_762
	v_max_f32_e32 v0, v0, v0
	v_max_f32_e32 v122, v202, v202
	v_max_f32_e32 v143, v122, v0
	v_sub_f32_e32 v0, v202, v143
	v_mul_f32_e32 v0, 0x3e38aa3b, v0
	v_exp_f32_e32 v202, v0
	s_nop 0
	v_pk_mul_f32 v[186:187], v[142:143], v[202:203]
	v_pk_mul_f32 v[156:157], v[156:157], v[202:203] op_sel_hi:[1,0]
	v_pk_mul_f32 v[154:155], v[154:155], v[202:203] op_sel_hi:[1,0]
	v_pk_mul_f32 v[160:161], v[160:161], v[202:203] op_sel_hi:[1,0]
	v_pk_mul_f32 v[158:159], v[158:159], v[202:203] op_sel_hi:[1,0]
	v_pk_mul_f32 v[164:165], v[164:165], v[202:203] op_sel_hi:[1,0]
	v_pk_mul_f32 v[162:163], v[162:163], v[202:203] op_sel_hi:[1,0]
	v_pk_mul_f32 v[168:169], v[168:169], v[202:203] op_sel_hi:[1,0]
	v_pk_mul_f32 v[166:167], v[166:167], v[202:203] op_sel_hi:[1,0]
	v_mov_b32_e32 v202, v143
	v_mov_b32_e32 v142, v186
